# v75 + per-segment 1/count precomputed in the scan phase; phase 2a reads it instead of re-deriving it
# speedup vs baseline: 1.0076x; 1.0076x over previous
_Z7vq_mainPKfPKiS0_PfPhPdPi:
	s_load_dwordx4 s[4:7], s[0:1], 0x0
	s_load_dwordx2 s[22:23], s[0:1], 0x10
	s_load_dwordx2 s[20:21], s[0:1], 0x18
	s_load_dwordx4 s[12:15], s[0:1], 0x20
	s_load_dwordx2 s[10:11], s[0:1], 0x30
	s_and_b32 s3, s2, 7
	s_lshl_b32 s3, s3, 6
	s_lshr_b32 s16, s2, 3
	s_add_i32 s16, s16, s3
	s_lshr_b32 s18, s16, 5
	s_mov_b32 s19, 0
	s_and_b32 s28, s16, 31
	s_lshl_b32 s28, s28, 4
	s_add_i32 s29, s28, 1
	v_readfirstlane_b32 s17, v0
	v_and_b32_e32 v1, 63, v0
	v_lshlrev_b32_e32 v66, 4, v0
	s_lshr_b32 s17, s17, 6
	s_lshl_b32 s24, s17, 4
	s_lshl_b32 s30, s18, 15
	s_lshl_b32 s31, s18, 23
	v_add_u32_e32 v67, 0x1000, v66
	v_add_u32_e32 v68, 0x2000, v66
	v_add_u32_e32 v69, 0x3000, v66
	v_add_u32_e32 v70, 0x4000, v66
	v_add_u32_e32 v71, 0x5000, v66
	v_add_u32_e32 v72, 0x6000, v66
	v_add_u32_e32 v73, 0x7000, v66
	s_movk_i32 s9, 0x810
	s_mov_b32 s3, 0x8100
	s_mul_i32 s36, s29, 0x810
	v_mov_b32_e32 v141, s36
	v_sub_u32_e32 v141, 0, v141
	s_waitcnt lgkmcnt(0)
	s_add_u32 s34, s6, s30
	s_addc_u32 s35, s7, 0
	s_add_u32 s32, s4, s31
	s_addc_u32 s33, s5, 0
	global_load_dwordx4 v[74:77], v66, s[34:35]
	global_load_dwordx4 v[78:81], v67, s[34:35]
	global_load_dwordx4 v[82:85], v68, s[34:35]
	global_load_dwordx4 v[86:89], v69, s[34:35]
	global_load_dwordx4 v[90:93], v70, s[34:35]
	global_load_dwordx4 v[94:97], v71, s[34:35]
	global_load_dwordx4 v[98:101], v72, s[34:35]
	global_load_dwordx4 v[102:105], v73, s[34:35]
	v_and_b32_e32 v150, 15, v0
	v_or_b32_e32 v150, s24, v150
	v_and_b32_e32 v151, 48, v0
	v_lshl_or_b32 v150, v150, 10, v151
	global_load_dwordx4 v[62:65], v150, s[22:23] offset:0
	global_load_dwordx4 v[58:61], v150, s[22:23] offset:64
	global_load_dwordx4 v[54:57], v150, s[22:23] offset:128
	global_load_dwordx4 v[50:53], v150, s[22:23] offset:192
	global_load_dwordx4 v[46:49], v150, s[22:23] offset:256
	global_load_dwordx4 v[42:45], v150, s[22:23] offset:320
	global_load_dwordx4 v[38:41], v150, s[22:23] offset:384
	global_load_dwordx4 v[34:37], v150, s[22:23] offset:448
	global_load_dwordx4 v[30:33], v150, s[22:23] offset:512
	global_load_dwordx4 v[26:29], v150, s[22:23] offset:576
	global_load_dwordx4 v[22:25], v150, s[22:23] offset:640
	global_load_dwordx4 v[18:21], v150, s[22:23] offset:704
	global_load_dwordx4 v[14:17], v150, s[22:23] offset:768
	global_load_dwordx4 v[10:13], v150, s[22:23] offset:832
	global_load_dwordx4 v[6:9], v150, s[22:23] offset:896
	global_load_dwordx4 v[2:5], v150, s[22:23] offset:960
	v_and_b32_e32 v138, 15, v0
	v_lshlrev_b32_e32 v139, 2, v1
	v_bfe_u32 v140, v0, 4, 2
	v_mov_b32_e32 v142, 1
	v_mov_b32_e32 v143, 4
	v_mov_b32_e32 v144, 0x11100
	v_lshlrev_b32_e32 v145, 8, v0
	v_lshlrev_b32_e32 v148, 3, v0
	v_mov_b32_e32 v152, 0
	v_mov_b32_e32 v153, 0
	ds_write_b64 v148, v[152:153] offset:32768
	ds_write_b64 v148, v[152:153] offset:34832
	ds_write_b64 v148, v[152:153] offset:36896
	ds_write_b64 v148, v[152:153] offset:38960
	ds_write_b64 v148, v[152:153] offset:41024
	ds_write_b64 v148, v[152:153] offset:43088
	ds_write_b64 v148, v[152:153] offset:45152
	ds_write_b64 v148, v[152:153] offset:47216
	ds_write_b64 v148, v[152:153] offset:49280
	ds_write_b64 v148, v[152:153] offset:51344
	ds_write_b64 v148, v[152:153] offset:53408
	ds_write_b64 v148, v[152:153] offset:55472
	ds_write_b64 v148, v[152:153] offset:57536
	ds_write_b64 v148, v[152:153] offset:59600
	ds_write_b64 v148, v[152:153] offset:61664
	ds_write_b64 v148, v[152:153] offset:63728
	v_cmp_gt_u32_e32 vcc, 16, v0
	s_and_saveexec_b64 s[30:31], vcc
	v_mul_u32_u24_e32 v151, 0x810, v0
	ds_write_b64 v151, v[152:153] offset:34816
	v_mov_b32_e32 v150, 0x11540
	v_mov_b32_e32 v149, 8
	ds_write_b32 v150, v149
	s_mov_b64 exec, s[30:31]
	s_waitcnt lgkmcnt(0)
	s_barrier
	s_waitcnt vmcnt(16)
	v_mad_u32_u24 v74, v74, s9, v141
	v_mad_u32_u24 v75, v75, s9, v141
	v_mad_u32_u24 v76, v76, s9, v141
	v_mad_u32_u24 v77, v77, s9, v141
	v_mad_u32_u24 v78, v78, s9, v141
	v_mad_u32_u24 v79, v79, s9, v141
	v_mad_u32_u24 v80, v80, s9, v141
	v_mad_u32_u24 v81, v81, s9, v141
	v_mad_u32_u24 v82, v82, s9, v141
	v_mad_u32_u24 v83, v83, s9, v141
	v_mad_u32_u24 v84, v84, s9, v141
	v_mad_u32_u24 v85, v85, s9, v141
	v_mad_u32_u24 v86, v86, s9, v141
	v_mad_u32_u24 v87, v87, s9, v141
	v_mad_u32_u24 v88, v88, s9, v141
	v_mad_u32_u24 v89, v89, s9, v141
	v_mad_u32_u24 v90, v90, s9, v141
	v_mad_u32_u24 v91, v91, s9, v141
	v_mad_u32_u24 v92, v92, s9, v141
	v_mad_u32_u24 v93, v93, s9, v141
	v_mad_u32_u24 v94, v94, s9, v141
	v_mad_u32_u24 v95, v95, s9, v141
	v_mad_u32_u24 v96, v96, s9, v141
	v_mad_u32_u24 v97, v97, s9, v141
	v_mad_u32_u24 v98, v98, s9, v141
	v_mad_u32_u24 v99, v99, s9, v141
	v_mad_u32_u24 v100, v100, s9, v141
	v_mad_u32_u24 v101, v101, s9, v141
	v_mad_u32_u24 v102, v102, s9, v141
	v_mad_u32_u24 v103, v103, s9, v141
	v_mad_u32_u24 v104, v104, s9, v141
	v_mad_u32_u24 v105, v105, s9, v141
	v_cmp_gt_u32_e64 s[36:37], s3, v74
	v_cmp_gt_u32_e64 s[38:39], s3, v75
	v_cmp_gt_u32_e64 s[40:41], s3, v76
	v_cmp_gt_u32_e64 s[42:43], s3, v77
	v_cmp_gt_u32_e64 s[44:45], s3, v78
	v_cmp_gt_u32_e64 s[46:47], s3, v79
	v_cmp_gt_u32_e64 s[48:49], s3, v80
	v_cmp_gt_u32_e64 s[50:51], s3, v81
	v_cmp_gt_u32_e64 s[52:53], s3, v82
	v_cmp_gt_u32_e64 s[54:55], s3, v83
	v_cmp_gt_u32_e64 s[56:57], s3, v84
	v_cmp_gt_u32_e64 s[58:59], s3, v85
	v_cmp_gt_u32_e64 s[60:61], s3, v86
	v_cmp_gt_u32_e64 s[62:63], s3, v87
	v_cmp_gt_u32_e64 s[64:65], s3, v88
	v_cmp_gt_u32_e64 s[66:67], s3, v89
	v_cmp_gt_u32_e64 s[68:69], s3, v90
	v_cmp_gt_u32_e64 s[70:71], s3, v91
	v_cmp_gt_u32_e64 s[72:73], s3, v92
	v_cmp_gt_u32_e64 s[74:75], s3, v93
	v_cmp_gt_u32_e64 s[76:77], s3, v94
	v_cmp_gt_u32_e64 s[78:79], s3, v95
	v_cmp_gt_u32_e64 s[80:81], s3, v96
	v_cmp_gt_u32_e64 s[82:83], s3, v97
	v_cmp_gt_u32_e64 s[84:85], s3, v98
	v_cmp_gt_u32_e64 s[86:87], s3, v99
	v_cmp_gt_u32_e64 s[88:89], s3, v100
	v_cmp_gt_u32_e64 s[90:91], s3, v101
	v_cmp_gt_u32_e64 s[92:93], s3, v102
	v_cmp_gt_u32_e64 s[94:95], s3, v103
	v_cmp_gt_u32_e64 s[96:97], s3, v104
	v_cmp_gt_u32_e64 s[98:99], s3, v105
	s_mov_b64 exec, s[36:37]
	ds_add_u32 v74, v142 offset:34816
	s_mov_b64 exec, s[38:39]
	ds_add_u32 v75, v142 offset:34816
	s_mov_b64 exec, s[40:41]
	ds_add_u32 v76, v142 offset:34816
	s_mov_b64 exec, s[42:43]
	ds_add_u32 v77, v142 offset:34816
	s_mov_b64 exec, s[44:45]
	ds_add_u32 v78, v142 offset:34816
	s_mov_b64 exec, s[46:47]
	ds_add_u32 v79, v142 offset:34816
	s_mov_b64 exec, s[48:49]
	ds_add_u32 v80, v142 offset:34816
	s_mov_b64 exec, s[50:51]
	ds_add_u32 v81, v142 offset:34816
	s_mov_b64 exec, s[52:53]
	ds_add_u32 v82, v142 offset:34816
	s_mov_b64 exec, s[54:55]
	ds_add_u32 v83, v142 offset:34816
	s_mov_b64 exec, s[56:57]
	ds_add_u32 v84, v142 offset:34816
	s_mov_b64 exec, s[58:59]
	ds_add_u32 v85, v142 offset:34816
	s_mov_b64 exec, s[60:61]
	ds_add_u32 v86, v142 offset:34816
	s_mov_b64 exec, s[62:63]
	ds_add_u32 v87, v142 offset:34816
	s_mov_b64 exec, s[64:65]
	ds_add_u32 v88, v142 offset:34816
	s_mov_b64 exec, s[66:67]
	ds_add_u32 v89, v142 offset:34816
	s_mov_b64 exec, s[68:69]
	ds_add_u32 v90, v142 offset:34816
	s_mov_b64 exec, s[70:71]
	ds_add_u32 v91, v142 offset:34816
	s_mov_b64 exec, s[72:73]
	ds_add_u32 v92, v142 offset:34816
	s_mov_b64 exec, s[74:75]
	ds_add_u32 v93, v142 offset:34816
	s_mov_b64 exec, s[76:77]
	ds_add_u32 v94, v142 offset:34816
	s_mov_b64 exec, s[78:79]
	ds_add_u32 v95, v142 offset:34816
	s_mov_b64 exec, s[80:81]
	ds_add_u32 v96, v142 offset:34816
	s_mov_b64 exec, s[82:83]
	ds_add_u32 v97, v142 offset:34816
	s_mov_b64 exec, s[84:85]
	ds_add_u32 v98, v142 offset:34816
	s_mov_b64 exec, s[86:87]
	ds_add_u32 v99, v142 offset:34816
	s_mov_b64 exec, s[88:89]
	ds_add_u32 v100, v142 offset:34816
	s_mov_b64 exec, s[90:91]
	ds_add_u32 v101, v142 offset:34816
	s_mov_b64 exec, s[92:93]
	ds_add_u32 v102, v142 offset:34816
	s_mov_b64 exec, s[94:95]
	ds_add_u32 v103, v142 offset:34816
	s_mov_b64 exec, s[96:97]
	ds_add_u32 v104, v142 offset:34816
	s_mov_b64 exec, s[98:99]
	ds_add_u32 v105, v142 offset:34816
	s_mov_b64 exec, -1
	s_waitcnt lgkmcnt(0)
	s_barrier
	v_and_b32_e32 v67, 15, v0
	v_mul_u32_u24_e32 v67, 0x810, v67
	ds_read_b32 v68, v67 offset:34816
	s_waitcnt lgkmcnt(0)
	v_mov_b32_e32 v69, v68
	s_nop 1
	v_add_u32_dpp v69, v69, v69 row_shr:1 row_mask:0xf bank_mask:0xf bound_ctrl:1
	s_nop 1
	v_add_u32_dpp v69, v69, v69 row_shr:2 row_mask:0xf bank_mask:0xf bound_ctrl:1
	s_nop 1
	v_add_u32_dpp v69, v69, v69 row_shr:4 row_mask:0xf bank_mask:0xf bound_ctrl:1
	s_nop 1
	v_add_u32_dpp v69, v69, v69 row_shr:8 row_mask:0xf bank_mask:0xf bound_ctrl:1
	s_nop 1
	v_sub_u32_e32 v70, v69, v68
	v_lshlrev_b32_e32 v70, 2, v70
	v_readlane_b32 s8, v69, 15
	s_cmp_lg_u32 s17, 0
	s_cbranch_scc1 .Lfront_nocursor
	v_cmp_gt_u32_e32 vcc, 16, v1
	s_and_saveexec_b64 s[30:31], vcc
	ds_write_b32 v67, v70 offset:34820
	v_lshl_add_u32 v71, v1, 2, v144
	ds_write_b32 v71, v68
	v_max_i32_e32 v150, 1, v68
	v_cvt_f32_u32_e32 v150, v150
	v_div_scale_f32 v151, s[100:101], v150, v150, 1.0
	v_rcp_f32_e32 v152, v151
	v_div_scale_f32 v153, vcc, 1.0, v150, 1.0
	v_fma_f32 v154, -v151, v152, 1.0
	v_fmac_f32_e32 v152, v154, v152
	v_mul_f32_e32 v154, v153, v152
	v_fma_f32 v155, -v151, v154, v153
	v_fmac_f32_e32 v154, v155, v152
	v_fma_f32 v153, -v151, v154, v153
	v_div_fmas_f32 v155, v153, v152, v154
	v_div_fixup_f32 v156, v155, v150, 1.0
	ds_write_b32 v71, v156 offset:320
	s_mov_b64 exec, s[30:31]

.LBB0_118:
	s_waitcnt vmcnt(0)
	v_lshrrev_b32_e32 v67, 4, v0
	v_mov_b32_e32 v66, 0x11100
	v_lshl_or_b32 v66, v67, 2, v66
	s_waitcnt lgkmcnt(0)
	s_barrier
	ds_read_b32 v77, v66 offset:320
	v_mul_u32_u24_e32 v68, 0x102, v67
	v_lshlrev_b32_e32 v72, 3, v68
	v_lshl_add_u32 v68, v138, 3, v72
	v_add_u32_e32 v76, 0x8000, v68
	ds_read2_b64 v[68:71], v76 offset1:16
	v_mul_i32_i24_e32 v73, 0xfffffbf8, v67
	v_lshlrev_b32_e32 v66, 2, v138
	v_add3_u32 v78, v72, v73, v66
	ds_read2_b64 v[72:75], v76 offset0:32 offset1:48
	s_waitcnt lgkmcnt(1)
	v_cvt_f32_f64_e32 v68, v[68:69]
	v_cvt_f32_f64_e32 v69, v[70:71]
	v_mul_f32_e32 v68, v77, v68
	v_mul_f32_e32 v69, v77, v69
	v_fma_f32 v79, v68, v68, 0
	ds_write2_b32 v78, v68, v69 offset1:16
	s_waitcnt lgkmcnt(1)
	v_cvt_f32_f64_e32 v68, v[72:73]
	v_fmac_f32_e32 v79, v69, v69
	v_mul_f32_e32 v72, v77, v68
	ds_read2_b64 v[68:71], v76 offset0:64 offset1:80
	v_cvt_f32_f64_e32 v73, v[74:75]
	v_fmac_f32_e32 v79, v72, v72
	v_mul_f32_e32 v73, v77, v73
	v_fmac_f32_e32 v79, v73, v73
	ds_write2_b32 v78, v72, v73 offset0:32 offset1:48
	ds_read2_b64 v[72:75], v76 offset0:96 offset1:112
	s_waitcnt lgkmcnt(2)
	v_cvt_f32_f64_e32 v68, v[68:69]
	v_cvt_f32_f64_e32 v69, v[70:71]
	v_mul_f32_e32 v68, v77, v68
	v_mul_f32_e32 v69, v77, v69
	v_fmac_f32_e32 v79, v68, v68
	ds_write2_b32 v78, v68, v69 offset0:64 offset1:80
	s_waitcnt lgkmcnt(1)
	v_cvt_f32_f64_e32 v68, v[72:73]
	v_fmac_f32_e32 v79, v69, v69
	v_mul_f32_e32 v72, v77, v68
	ds_read2_b64 v[68:71], v76 offset0:128 offset1:144
	v_cvt_f32_f64_e32 v73, v[74:75]
	v_fmac_f32_e32 v79, v72, v72
	v_mul_f32_e32 v73, v77, v73
	v_fmac_f32_e32 v79, v73, v73
	ds_write2_b32 v78, v72, v73 offset0:96 offset1:112
	ds_read2_b64 v[72:75], v76 offset0:160 offset1:176
	s_waitcnt lgkmcnt(2)
	v_cvt_f32_f64_e32 v68, v[68:69]
	v_cvt_f32_f64_e32 v69, v[70:71]
	v_mul_f32_e32 v68, v77, v68
	v_mul_f32_e32 v69, v77, v69
	v_fmac_f32_e32 v79, v68, v68
	ds_write2_b32 v78, v68, v69 offset0:128 offset1:144
	s_waitcnt lgkmcnt(1)
	v_cvt_f32_f64_e32 v68, v[72:73]
	v_fmac_f32_e32 v79, v69, v69
	v_mul_f32_e32 v72, v77, v68
	ds_read2_b64 v[68:71], v76 offset0:192 offset1:208
	v_cvt_f32_f64_e32 v73, v[74:75]
	v_fmac_f32_e32 v79, v72, v72
	v_mul_f32_e32 v73, v77, v73
	v_fmac_f32_e32 v79, v73, v73
	ds_write2_b32 v78, v72, v73 offset0:160 offset1:176
	ds_read2_b64 v[72:75], v76 offset0:224 offset1:240
	s_waitcnt lgkmcnt(2)
	v_cvt_f32_f64_e32 v68, v[68:69]
	v_cvt_f32_f64_e32 v69, v[70:71]
	v_mul_f32_e32 v68, v77, v68
	v_mul_f32_e32 v69, v77, v69
	v_fmac_f32_e32 v79, v68, v68
	ds_write2_b32 v78, v68, v69 offset0:192 offset1:208
	s_waitcnt lgkmcnt(1)
	v_cvt_f32_f64_e32 v68, v[72:73]
	v_fmac_f32_e32 v79, v69, v69
	v_mul_f32_e32 v68, v77, v68
	v_cvt_f32_f64_e32 v69, v[74:75]
	v_fmac_f32_e32 v79, v68, v68
	v_mul_f32_e32 v69, v77, v69
	v_fmac_f32_e32 v79, v69, v69
	ds_write2_b32 v78, v68, v69 offset0:224 offset1:240
	v_cmp_eq_u32_e32 vcc, 0, v138
	v_add_f32_dpp v68, v79, v79 quad_perm:[1,0,3,2] row_mask:0xf bank_mask:0xf bound_ctrl:1
	s_nop 1
	v_add_f32_dpp v68, v68, v68 quad_perm:[2,3,0,1] row_mask:0xf bank_mask:0xf bound_ctrl:1
	s_nop 1
	v_add_f32_dpp v68, v68, v68 row_half_mirror row_mask:0xf bank_mask:0xf bound_ctrl:1
	s_nop 1
	v_mov_b32_dpp v69, v68 row_mirror row_mask:0xf bank_mask:0xf bound_ctrl:1
	s_and_saveexec_b64 s[0:1], vcc
	v_mov_b32_e32 v70, 0x11200
	v_lshl_or_b32 v67, v67, 2, v70
	v_add_f32_e32 v68, v68, v69
	ds_write_b32 v67, v68
	s_or_b64 exec, exec, s[0:1]
	v_lshlrev_b32_e32 v67, 2, v140
	s_movk_i32 s0, 0x408
	v_mad_u32_u24 v67, v138, s0, v67
	s_waitcnt lgkmcnt(0)
	s_barrier
	ds_read2_b32 v[68:69], v67 offset1:4
	ds_read2_b32 v[70:71], v67 offset0:64 offset1:68
	ds_read2_b32 v[72:73], v67 offset0:192 offset1:196
	s_lshl_b32 s29, s17, 2
	s_lshl_b32 s0, s24, 2
	s_waitcnt lgkmcnt(2)
	v_mfma_f32_16x16x4_f32 a[0:3], v68, v62, 0
	s_add_i32 s0, s0, 0x10100
	s_waitcnt lgkmcnt(1)
	v_mfma_f32_16x16x4_f32 a[4:7], v70, v63, 0
	ds_read2_b32 v[62:63], v67 offset0:128 offset1:132
	s_waitcnt lgkmcnt(0)
	v_mfma_f32_16x16x4_f32 a[0:3], v62, v64, a[0:3]
	v_mfma_f32_16x16x4_f32 a[4:7], v72, v65, a[4:7]
	v_mfma_f32_16x16x4_f32 a[0:3], v69, v58, a[0:3]
	v_mfma_f32_16x16x4_f32 a[4:7], v71, v59, a[4:7]
	ds_read2_b32 v[58:59], v67 offset0:8 offset1:12
	v_mfma_f32_16x16x4_f32 a[0:3], v63, v60, a[0:3]
	ds_read2_b32 v[62:63], v67 offset0:200 offset1:204
	v_mfma_f32_16x16x4_f32 a[4:7], v73, v61, a[4:7]
	ds_read2_b32 v[60:61], v67 offset0:72 offset1:76
	s_waitcnt lgkmcnt(2)
	v_mfma_f32_16x16x4_f32 a[0:3], v58, v54, a[0:3]
	s_waitcnt lgkmcnt(0)
	v_mfma_f32_16x16x4_f32 a[4:7], v60, v55, a[4:7]
	ds_read2_b32 v[54:55], v67 offset0:136 offset1:140
	s_waitcnt lgkmcnt(0)
	v_mfma_f32_16x16x4_f32 a[0:3], v54, v56, a[0:3]
	v_mfma_f32_16x16x4_f32 a[4:7], v62, v57, a[4:7]
	v_mfma_f32_16x16x4_f32 a[0:3], v59, v50, a[0:3]
	v_mfma_f32_16x16x4_f32 a[4:7], v61, v51, a[4:7]
	ds_read2_b32 v[50:51], v67 offset0:16 offset1:20
	v_mfma_f32_16x16x4_f32 a[0:3], v55, v52, a[0:3]
	ds_read2_b32 v[54:55], v67 offset0:208 offset1:212
	v_mfma_f32_16x16x4_f32 a[4:7], v63, v53, a[4:7]
	ds_read2_b32 v[52:53], v67 offset0:80 offset1:84
	s_waitcnt lgkmcnt(2)
	v_mfma_f32_16x16x4_f32 a[0:3], v50, v46, a[0:3]
	s_waitcnt lgkmcnt(0)
	v_mfma_f32_16x16x4_f32 a[4:7], v52, v47, a[4:7]
	ds_read2_b32 v[46:47], v67 offset0:144 offset1:148
	s_waitcnt lgkmcnt(0)
	v_mfma_f32_16x16x4_f32 a[0:3], v46, v48, a[0:3]
	v_mfma_f32_16x16x4_f32 a[4:7], v54, v49, a[4:7]
	v_mfma_f32_16x16x4_f32 a[0:3], v51, v42, a[0:3]
	v_mfma_f32_16x16x4_f32 a[4:7], v53, v43, a[4:7]
	ds_read2_b32 v[42:43], v67 offset0:24 offset1:28
	v_mfma_f32_16x16x4_f32 a[0:3], v47, v44, a[0:3]
	ds_read2_b32 v[46:47], v67 offset0:216 offset1:220
	v_mfma_f32_16x16x4_f32 a[4:7], v55, v45, a[4:7]
	ds_read2_b32 v[44:45], v67 offset0:88 offset1:92
	s_waitcnt lgkmcnt(2)
	v_mfma_f32_16x16x4_f32 a[0:3], v42, v38, a[0:3]
	s_waitcnt lgkmcnt(0)
	v_mfma_f32_16x16x4_f32 a[4:7], v44, v39, a[4:7]
	ds_read2_b32 v[38:39], v67 offset0:152 offset1:156
	s_waitcnt lgkmcnt(0)
	v_mfma_f32_16x16x4_f32 a[0:3], v38, v40, a[0:3]
	v_mfma_f32_16x16x4_f32 a[4:7], v46, v41, a[4:7]
	v_mfma_f32_16x16x4_f32 a[0:3], v43, v34, a[0:3]
	v_mfma_f32_16x16x4_f32 a[4:7], v45, v35, a[4:7]
	ds_read2_b32 v[34:35], v67 offset0:32 offset1:36
	v_mfma_f32_16x16x4_f32 a[0:3], v39, v36, a[0:3]
	ds_read2_b32 v[38:39], v67 offset0:224 offset1:228
	v_mfma_f32_16x16x4_f32 a[4:7], v47, v37, a[4:7]
	ds_read2_b32 v[36:37], v67 offset0:96 offset1:100
	s_waitcnt lgkmcnt(2)
	v_mfma_f32_16x16x4_f32 a[0:3], v34, v30, a[0:3]
	s_waitcnt lgkmcnt(0)
	v_mfma_f32_16x16x4_f32 a[4:7], v36, v31, a[4:7]
	ds_read2_b32 v[30:31], v67 offset0:160 offset1:164
	s_waitcnt lgkmcnt(0)
	v_mfma_f32_16x16x4_f32 a[0:3], v30, v32, a[0:3]
	v_mfma_f32_16x16x4_f32 a[4:7], v38, v33, a[4:7]
	v_mfma_f32_16x16x4_f32 a[0:3], v35, v26, a[0:3]
	v_mfma_f32_16x16x4_f32 a[4:7], v37, v27, a[4:7]
	ds_read2_b32 v[26:27], v67 offset0:40 offset1:44
	v_mfma_f32_16x16x4_f32 a[0:3], v31, v28, a[0:3]
	ds_read2_b32 v[30:31], v67 offset0:232 offset1:236
	v_mfma_f32_16x16x4_f32 a[4:7], v39, v29, a[4:7]
	ds_read2_b32 v[28:29], v67 offset0:104 offset1:108
	s_waitcnt lgkmcnt(2)
	v_mfma_f32_16x16x4_f32 a[0:3], v26, v22, a[0:3]
	s_waitcnt lgkmcnt(0)
	v_mfma_f32_16x16x4_f32 a[4:7], v28, v23, a[4:7]
	ds_read2_b32 v[22:23], v67 offset0:168 offset1:172
	s_waitcnt lgkmcnt(0)
	v_mfma_f32_16x16x4_f32 a[0:3], v22, v24, a[0:3]
	v_mfma_f32_16x16x4_f32 a[4:7], v30, v25, a[4:7]
	v_mfma_f32_16x16x4_f32 a[0:3], v27, v18, a[0:3]
	v_mfma_f32_16x16x4_f32 a[4:7], v29, v19, a[4:7]
	ds_read2_b32 v[18:19], v67 offset0:48 offset1:52
	v_mfma_f32_16x16x4_f32 a[0:3], v23, v20, a[0:3]
	ds_read2_b32 v[22:23], v67 offset0:240 offset1:244
	v_mfma_f32_16x16x4_f32 a[4:7], v31, v21, a[4:7]
	ds_read2_b32 v[20:21], v67 offset0:112 offset1:116
	s_waitcnt lgkmcnt(2)
	v_mfma_f32_16x16x4_f32 a[0:3], v18, v14, a[0:3]
	s_waitcnt lgkmcnt(0)
	v_mfma_f32_16x16x4_f32 a[4:7], v20, v15, a[4:7]
	ds_read2_b32 v[14:15], v67 offset0:176 offset1:180
	s_waitcnt lgkmcnt(0)
	v_mfma_f32_16x16x4_f32 a[0:3], v14, v16, a[0:3]
	v_mfma_f32_16x16x4_f32 a[4:7], v22, v17, a[4:7]
	v_mfma_f32_16x16x4_f32 a[0:3], v19, v10, a[0:3]
	v_mfma_f32_16x16x4_f32 a[4:7], v21, v11, a[4:7]
	ds_read2_b32 v[10:11], v67 offset0:56 offset1:60
	v_mfma_f32_16x16x4_f32 a[0:3], v15, v12, a[0:3]
	ds_read2_b32 v[14:15], v67 offset0:248 offset1:252
	v_mfma_f32_16x16x4_f32 a[4:7], v23, v13, a[4:7]
	ds_read2_b32 v[12:13], v67 offset0:120 offset1:124
	s_waitcnt lgkmcnt(2)
	v_mfma_f32_16x16x4_f32 a[0:3], v10, v6, a[0:3]
	s_waitcnt lgkmcnt(0)
	v_mfma_f32_16x16x4_f32 a[4:7], v12, v7, a[4:7]
	ds_read2_b32 v[6:7], v67 offset0:184 offset1:188
	s_waitcnt lgkmcnt(0)
	v_mfma_f32_16x16x4_f32 a[0:3], v6, v8, a[0:3]
	v_mfma_f32_16x16x4_f32 a[4:7], v14, v9, a[4:7]
	v_mfma_f32_16x16x4_f32 a[0:3], v11, v2, a[0:3]
	v_mov_b32_e32 v2, 0x11300
	v_lshl_add_u32 v2, v134, 2, v2
	ds_read_b32 v2, v2
	v_mfma_f32_16x16x4_f32 a[4:7], v13, v3, a[4:7]
	v_lshlrev_b32_e32 v3, 10, v140
	v_add3_u32 v3, s0, v66, v3
	v_mfma_f32_16x16x4_f32 a[0:3], v7, v4, a[0:3]
	v_or_b32_e32 v7, s29, v140
	v_lshl_or_b32 v4, v7, 8, v66
	v_add_u32_e32 v4, 0x10100, v4
	v_mfma_f32_16x16x4_f32 a[4:7], v15, v5, a[4:7]
	s_nop 9
	v_accvgpr_read_b32 v5, a0
	v_accvgpr_read_b32 v6, a1
	v_accvgpr_read_b32 v8, a2
	v_accvgpr_read_b32 v9, a3
	v_accvgpr_read_b32 v70, a4
	v_accvgpr_read_b32 v71, a5
	v_accvgpr_read_b32 v72, a6
	v_accvgpr_read_b32 v73, a7
	v_add_f32_e32 v5, v5, v70
	v_add_f32_e32 v6, v6, v71
	v_add_f32_e32 v8, v8, v72
	v_add_f32_e32 v9, v9, v73
	s_waitcnt lgkmcnt(0)
	v_fma_f32 v5, -2.0, v5, v2
	v_fma_f32 v6, -2.0, v6, v2
	v_fma_f32 v8, -2.0, v8, v2
	v_fmac_f32_e32 v2, -2.0, v9
	ds_write2st64_b32 v3, v5, v6 offset1:1
	ds_write2st64_b32 v3, v8, v2 offset0:2 offset1:3
	s_waitcnt lgkmcnt(0)
	s_barrier
	ds_read2_b32 v[2:3], v4 offset1:16
	ds_read2_b32 v[4:5], v4 offset0:32 offset1:48
	v_or_b32_e32 v6, 16, v138
	v_or_b32_e32 v8, 32, v138
	v_or_b32_e32 v9, 48, v138
	s_waitcnt lgkmcnt(1)
	v_cmp_lt_f32_e32 vcc, v3, v2
	s_nop 1
	v_cndmask_b32_e32 v10, v2, v3, vcc
	v_cndmask_b32_e32 v6, v138, v6, vcc
	s_waitcnt lgkmcnt(0)
	v_cmp_lt_f32_e32 vcc, v4, v10
	s_nop 1
	v_cndmask_b32_e32 v10, v10, v4, vcc
	v_cndmask_b32_e32 v8, v6, v8, vcc
	v_cmp_lt_f32_e32 vcc, v5, v10
	s_nop 1
	v_cndmask_b32_e32 v6, v10, v5, vcc
	v_cndmask_b32_e32 v14, v8, v9, vcc
	s_nop 0
	v_mov_b32_dpp v9, v6 quad_perm:[1,0,3,2] row_mask:0xf bank_mask:0xf bound_ctrl:1
	v_mov_b32_dpp v8, v14 quad_perm:[1,0,3,2] row_mask:0xf bank_mask:0xf bound_ctrl:1
	v_cmp_gt_f32_e64 s[4:5], v6, v9
	v_cmp_ngt_f32_e32 vcc, v6, v9
	s_and_saveexec_b64 s[6:7], vcc
	v_cmp_eq_f32_e32 vcc, v6, v9
	v_cmp_lt_i32_e64 s[0:1], v8, v14
	s_and_b64 s[0:1], vcc, s[0:1]
	s_andn2_b64 s[4:5], s[4:5], exec
	s_and_b64 s[0:1], s[0:1], exec
	s_or_b64 s[4:5], s[4:5], s[0:1]
	s_or_b64 exec, exec, s[6:7]
	s_and_saveexec_b64 s[0:1], s[4:5]
	v_mov_b32_e32 v6, v9
	v_mov_b32_e32 v14, v8
	s_or_b64 exec, exec, s[0:1]
	v_mov_b32_dpp v9, v6 quad_perm:[2,3,0,1] row_mask:0xf bank_mask:0xf bound_ctrl:1
	v_mov_b32_dpp v8, v14 quad_perm:[2,3,0,1] row_mask:0xf bank_mask:0xf bound_ctrl:1
	v_cmp_gt_f32_e64 s[4:5], v6, v9
	v_cmp_ngt_f32_e32 vcc, v6, v9
	s_and_saveexec_b64 s[6:7], vcc
	v_cmp_eq_f32_e32 vcc, v6, v9
	v_cmp_lt_i32_e64 s[0:1], v8, v14
	s_and_b64 s[0:1], vcc, s[0:1]
	s_andn2_b64 s[4:5], s[4:5], exec
	s_and_b64 s[0:1], s[0:1], exec
	s_or_b64 s[4:5], s[4:5], s[0:1]
	s_or_b64 exec, exec, s[6:7]
	s_and_saveexec_b64 s[0:1], s[4:5]
	v_mov_b32_e32 v6, v9
	v_mov_b32_e32 v14, v8
	s_or_b64 exec, exec, s[0:1]
	v_mov_b32_dpp v9, v6 row_half_mirror row_mask:0xf bank_mask:0xf bound_ctrl:1
	v_mov_b32_dpp v8, v14 row_half_mirror row_mask:0xf bank_mask:0xf bound_ctrl:1
	v_cmp_gt_f32_e64 s[4:5], v6, v9
	v_cmp_ngt_f32_e32 vcc, v6, v9
	s_and_saveexec_b64 s[6:7], vcc
	v_cmp_eq_f32_e32 vcc, v6, v9
	v_cmp_lt_i32_e64 s[0:1], v8, v14
	s_and_b64 s[0:1], vcc, s[0:1]
	s_andn2_b64 s[4:5], s[4:5], exec
	s_and_b64 s[0:1], s[0:1], exec
	s_or_b64 s[4:5], s[4:5], s[0:1]
	s_or_b64 exec, exec, s[6:7]
	s_and_saveexec_b64 s[0:1], s[4:5]
	v_mov_b32_e32 v6, v9
	v_mov_b32_e32 v14, v8
	s_or_b64 exec, exec, s[0:1]
	v_mov_b32_dpp v8, v6 row_mirror row_mask:0xf bank_mask:0xf bound_ctrl:1
	v_mov_b32_dpp v9, v14 row_mirror row_mask:0xf bank_mask:0xf bound_ctrl:1
	v_cmp_gt_f32_e64 s[4:5], v6, v8
	v_cmp_ngt_f32_e32 vcc, v6, v8
	s_and_saveexec_b64 s[6:7], vcc
	v_cmp_eq_f32_e32 vcc, v6, v8
	v_cmp_lt_i32_e64 s[0:1], v9, v14
	s_and_b64 s[0:1], vcc, s[0:1]
	s_andn2_b64 s[4:5], s[4:5], exec
	s_and_b64 s[0:1], s[0:1], exec
	s_or_b64 s[4:5], s[4:5], s[0:1]
	s_or_b64 exec, exec, s[6:7]
	s_and_saveexec_b64 s[0:1], s[4:5]
	v_mov_b32_e32 v6, v8
	v_mov_b32_e32 v14, v9
	s_or_b64 exec, exec, s[0:1]
	v_mov_b32_e32 v8, 0x11300
	v_lshl_or_b32 v8, v1, 2, v8
	ds_read_b32 v8, v8
	v_mov_b32_e32 v9, 0x11200
	v_lshl_add_u32 v7, v7, 2, v9
	ds_read_b32 v9, v7
	v_mov_b32_e32 v13, 0x260
	s_waitcnt lgkmcnt(1)
	v_mov_b32_dpp v7, v8 quad_perm:[1,0,3,2] row_mask:0xf bank_mask:0xf bound_ctrl:1
	v_max_f32_e32 v8, v8, v8
	v_max_f32_e32 v7, v7, v7
	v_max_f32_e32 v7, v8, v7
	v_lshlrev_b32_e32 v18, 2, v139
	v_mov_b32_e32 v19, 0
	v_mov_b32_dpp v8, v7 quad_perm:[2,3,0,1] row_mask:0xf bank_mask:0xf bound_ctrl:1
	v_max_f32_e32 v8, v8, v8
	v_max_f32_e32 v7, v7, v8
	s_mov_b32 s25, 0
	s_mov_b32 s26, s25
	v_mov_b32_dpp v8, v7 row_half_mirror row_mask:0xf bank_mask:0xf bound_ctrl:1
	v_max_f32_e32 v8, v8, v8
	v_max_f32_e32 v7, v7, v8
	s_nop 1
	v_mov_b32_dpp v8, v7 row_mirror row_mask:0xf bank_mask:0xf bound_ctrl:1
	v_max_f32_e32 v8, v8, v8
	v_max_f32_e32 v7, v7, v8
	s_nop 0
	v_readlane_b32 s4, v7, 32
	v_readlane_b32 s5, v7, 48
	v_readlane_b32 s0, v7, 0
	v_readlane_b32 s1, v7, 16
	v_max_f32_e64 v7, s5, s5
	v_max_f32_e64 v8, s4, s4
	v_max_f32_e32 v7, v8, v7
	v_mov_b32_e32 v8, s1
	v_max3_f32 v8, s0, v8, v7
	s_mov_b32 s0, 0x3f800347
	s_mov_b32 s1, 0x3f8020c5
	s_waitcnt lgkmcnt(0)
	v_pk_mul_f32 v[8:9], v[8:9], s[0:1]
	s_mov_b32 s4, 0xf800000
	v_mul_f32_e32 v7, 0x4f800000, v9
	v_cmp_gt_f32_e32 vcc, s4, v9
	s_nop 1
	v_cndmask_b32_e32 v7, v9, v7, vcc
	v_sqrt_f32_e32 v10, v7
	s_nop 0
	v_add_u32_e32 v11, -1, v10
	v_fma_f32 v12, -v11, v10, v7
	v_cmp_ge_f32_e64 s[0:1], 0, v12
	v_add_u32_e32 v12, 1, v10
	s_nop 0
	v_cndmask_b32_e64 v11, v10, v11, s[0:1]
	v_fma_f32 v10, -v12, v10, v7
	v_cmp_lt_f32_e64 s[0:1], 0, v10
	s_nop 1
	v_cndmask_b32_e64 v10, v11, v12, s[0:1]
	v_mul_f32_e32 v11, 0x37800000, v10
	v_cndmask_b32_e32 v10, v10, v11, vcc
	v_mul_f32_e32 v11, 0x4f800000, v8
	v_cmp_gt_f32_e32 vcc, s4, v8
	v_cmp_class_f32_e64 s[0:1], v7, v13
	s_nop 0
	v_cndmask_b32_e32 v11, v8, v11, vcc
	v_sqrt_f32_e32 v12, v11
	v_cndmask_b32_e64 v7, v10, v7, s[0:1]
	v_add_u32_e32 v10, -1, v12
	v_fma_f32 v15, -v10, v12, v11
	v_cmp_ge_f32_e64 s[0:1], 0, v15
	v_add_u32_e32 v15, 1, v12
	s_nop 0
	v_cndmask_b32_e64 v10, v12, v10, s[0:1]
	v_fma_f32 v12, -v15, v12, v11
	v_cmp_lt_f32_e64 s[0:1], 0, v12
	s_nop 1
	v_cndmask_b32_e64 v10, v10, v15, s[0:1]
	v_mul_f32_e32 v12, 0x37800000, v10
	v_cndmask_b32_e32 v10, v10, v12, vcc
	v_cmp_class_f32_e32 vcc, v11, v13
	s_mov_b32 s0, 0x380637bd
	s_mov_b32 s1, 0x350637bd
	v_cndmask_b32_e32 v10, v10, v11, vcc
	v_mul_f32_e32 v7, v7, v10
	v_mul_f32_e32 v7, 0x3f800347, v7
	v_pk_mul_f32 v[8:9], v[8:9], s[0:1]
	s_nop 0
	v_fmamk_f32 v7, v7, 0x3888509c, v9
	v_add_f32_e32 v7, v8, v7
	v_add_f32_e32 v7, 0xda24260, v7
	v_add_f32_e32 v6, v6, v7
	v_cmp_le_f32_e64 s[8:9], v2, v6
	v_cmp_le_f32_e64 s[6:7], v3, v6
	v_cmp_le_f32_e64 s[4:5], v4, v6
	v_lshl_add_u64 v[2:3], s[22:23], 0, v[18:19]
	s_and_b32 s19, s8, 0xffff
	s_lshl_b32 s22, s6, 16
	v_cmp_le_f32_e64 s[0:1], v5, v6
	s_or_b32 s24, s19, s22
	s_and_b32 s23, s4, 0xffff
	s_mov_b32 s22, s25
	s_or_b64 s[22:23], s[24:25], s[22:23]
	s_lshl_b32 s27, s0, 16
	s_or_b64 s[26:27], s[22:23], s[26:27]
	s_add_u32 s22, s26, -1
	s_addc_u32 s23, s27, -1
	s_and_b64 s[22:23], s[26:27], s[22:23]
	s_cmp_eq_u64 s[22:23], 0
	v_readlane_b32 s22, v14, 0
	s_cbranch_scc1 .LBB0_139
	s_lshl_b32 s19, s29, 2
	s_add_i32 s19, s19, 0x11100
	v_mov_b32_e32 v4, s19
	ds_read_b32 v4, v4
	s_mul_i32 s19, s17, 0x2040
	v_add_u32_e32 v8, s19, v135
	v_mov_b32_e32 v15, 0x7f800000
	s_waitcnt lgkmcnt(0)
	v_max_i32_e32 v4, 1, v4
	v_cvt_f64_u32_e32 v[12:13], v4
	v_div_scale_f64 v[16:17], s[30:31], v[12:13], v[12:13], 1.0
	v_rcp_f64_e32 v[20:21], v[16:17]
	v_div_scale_f64 v[22:23], vcc, 1.0, v[12:13], 1.0
	ds_read2st64_b64 v[4:7], v8 offset0:64 offset1:65
	ds_read2st64_b64 v[8:11], v8 offset0:66 offset1:67
	v_fma_f64 v[24:25], -v[16:17], v[20:21], 1.0
	v_fmac_f64_e32 v[20:21], v[20:21], v[24:25]
	v_fma_f64 v[24:25], -v[16:17], v[20:21], 1.0
	v_fmac_f64_e32 v[20:21], v[20:21], v[24:25]
	v_mul_f64 v[24:25], v[22:23], v[20:21]
	v_fma_f64 v[16:17], -v[16:17], v[24:25], v[22:23]
	v_div_fmas_f64 v[16:17], v[16:17], v[20:21], v[24:25]
	v_div_fixup_f64 v[12:13], v[16:17], v[12:13], 1.0
	s_waitcnt lgkmcnt(1)
	v_mul_f64 v[6:7], v[6:7], v[12:13]
	v_mul_f64 v[4:5], v[4:5], v[12:13]
	s_waitcnt lgkmcnt(0)
	v_mul_f64 v[8:9], v[8:9], v[12:13]
	v_mul_f64 v[10:11], v[12:13], v[10:11]
	v_mul_f64 v[12:13], v[6:7], v[6:7]
	v_fmac_f64_e32 v[12:13], v[4:5], v[4:5]
	v_fmac_f64_e32 v[12:13], v[8:9], v[8:9]
	v_fmac_f64_e32 v[12:13], v[10:11], v[10:11]
	s_nop 1
	v_mov_b32_dpp v16, v12 quad_perm:[1,0,3,2] row_mask:0xf bank_mask:0xf bound_ctrl:1
	v_mov_b32_dpp v17, v13 quad_perm:[1,0,3,2] row_mask:0xf bank_mask:0xf bound_ctrl:1
	v_add_f64 v[12:13], v[12:13], v[16:17]
	s_nop 1
	v_mov_b32_dpp v16, v12 quad_perm:[2,3,0,1] row_mask:0xf bank_mask:0xf bound_ctrl:1
	v_mov_b32_dpp v17, v13 quad_perm:[2,3,0,1] row_mask:0xf bank_mask:0xf bound_ctrl:1
	v_add_f64 v[12:13], v[12:13], v[16:17]
	s_nop 1
	v_mov_b32_dpp v16, v12 row_half_mirror row_mask:0xf bank_mask:0xf bound_ctrl:1
	v_mov_b32_dpp v17, v13 row_half_mirror row_mask:0xf bank_mask:0xf bound_ctrl:1
	v_add_f64 v[12:13], v[12:13], v[16:17]
	s_nop 1
	v_mov_b32_dpp v16, v12 row_mirror row_mask:0xf bank_mask:0xf bound_ctrl:1
	v_mov_b32_dpp v17, v13 row_mirror row_mask:0xf bank_mask:0xf bound_ctrl:1
	v_add_f64 v[12:13], v[12:13], v[16:17]
	s_nop 0
	v_readlane_b32 s19, v13, 16
	v_readlane_b32 s23, v12, 16
	v_readlane_b32 s31, v13, 0
	v_readlane_b32 s30, v12, 0
	v_mov_b32_e32 v16, s23
	v_mov_b32_e32 v17, s19
	v_readlane_b32 s19, v13, 48
	v_readlane_b32 s23, v12, 48
	v_add_f64 v[16:17], s[30:31], v[16:17]
	v_readlane_b32 s31, v13, 32
	v_readlane_b32 s30, v12, 32
	v_mov_b32_e32 v12, s23
	v_mov_b32_e32 v13, s19
	v_add_f64 v[12:13], s[30:31], v[12:13]
	v_add_f64 v[12:13], v[16:17], v[12:13]
